# baseline (speedup 1.0000x reference)
.LBB5_167:
	v_and_b32_e32 v83, 15, v12
	v_add_u32_e32 v84, s7, v82
	v_add_u32_e32 v85, 1, v12
	v_add_u32_e32 v86, 2, v12
	v_add_u32_e32 v87, 3, v12
	v_lshl_or_b32 v88, v83, 6, v186
	v_and_b32_e32 v89, 32, v84
	v_and_b32_e32 v85, 15, v85
	v_add_u32_e32 v90, 4, v84
	v_and_b32_e32 v86, 15, v86
	v_add_u32_e32 v91, 8, v84
	v_and_b32_e32 v87, 15, v87
	v_add_u32_e32 v84, 12, v84
	v_xad_u32 v88, v88, v89, v80
	v_lshl_add_u32 v83, v83, 2, v81
	v_lshl_or_b32 v89, v85, 6, v186
	v_lshl_add_u32 v92, v85, 2, v81
	v_lshl_or_b32 v93, v86, 6, v186
	v_lshl_add_u32 v96, v86, 2, v81
	v_lshl_or_b32 v94, v87, 6, v186
	v_and_b32_e32 v95, 32, v84
	v_lshl_add_u32 v101, v87, 2, v81
	ds_read_b128 v[84:87], v88
	ds_read_b32 v100, v83
	v_and_b32_e32 v90, 32, v90
	v_and_b32_e32 v91, 32, v91
	v_xad_u32 v83, v89, v90, v80
	v_xad_u32 v93, v93, v91, v80
	v_xad_u32 v97, v94, v95, v80
	ds_read_b128 v[88:91], v83
	ds_read_b32 v102, v92
	ds_read_b128 v[92:95], v93
	ds_read_b32 v104, v96
	ds_read_b128 v[96:99], v97
	ds_read_b32 v106, v101
	s_waitcnt lgkmcnt(7)
	v_cvt_f32_f16_e32 v108, v84
	v_cvt_f32_f16_sdwa v109, v84 dst_sel:DWORD dst_unused:UNUSED_PAD src0_sel:WORD_1
	v_cvt_f32_f16_e32 v84, v85
	v_cvt_f32_f16_sdwa v85, v85 dst_sel:DWORD dst_unused:UNUSED_PAD src0_sel:WORD_1
	v_cvt_f32_f16_e32 v110, v86
	v_cvt_f32_f16_sdwa v111, v86 dst_sel:DWORD dst_unused:UNUSED_PAD src0_sel:WORD_1
	v_cvt_f32_f16_e32 v86, v87
	v_cvt_f32_f16_sdwa v87, v87 dst_sel:DWORD dst_unused:UNUSED_PAD src0_sel:WORD_1
	s_waitcnt lgkmcnt(5)
	v_cvt_f32_f16_e32 v112, v88
	v_cvt_f32_f16_sdwa v113, v88 dst_sel:DWORD dst_unused:UNUSED_PAD src0_sel:WORD_1
	v_cvt_f32_f16_e32 v88, v89
	v_cvt_f32_f16_sdwa v89, v89 dst_sel:DWORD dst_unused:UNUSED_PAD src0_sel:WORD_1
	v_cvt_f32_f16_e32 v114, v90
	v_cvt_f32_f16_sdwa v115, v90 dst_sel:DWORD dst_unused:UNUSED_PAD src0_sel:WORD_1
	v_cvt_f32_f16_e32 v90, v91
	v_cvt_f32_f16_sdwa v91, v91 dst_sel:DWORD dst_unused:UNUSED_PAD src0_sel:WORD_1
	s_waitcnt lgkmcnt(3)
	v_cvt_f32_f16_e32 v116, v92
	v_cvt_f32_f16_sdwa v117, v92 dst_sel:DWORD dst_unused:UNUSED_PAD src0_sel:WORD_1
	v_cvt_f32_f16_e32 v92, v93
	v_cvt_f32_f16_sdwa v93, v93 dst_sel:DWORD dst_unused:UNUSED_PAD src0_sel:WORD_1
	v_cvt_f32_f16_e32 v118, v94
	v_cvt_f32_f16_sdwa v119, v94 dst_sel:DWORD dst_unused:UNUSED_PAD src0_sel:WORD_1
	v_cvt_f32_f16_e32 v94, v95
	v_cvt_f32_f16_sdwa v95, v95 dst_sel:DWORD dst_unused:UNUSED_PAD src0_sel:WORD_1
	s_waitcnt lgkmcnt(1)
	v_cvt_f32_f16_e32 v120, v96
	v_cvt_f32_f16_sdwa v121, v96 dst_sel:DWORD dst_unused:UNUSED_PAD src0_sel:WORD_1
	v_cvt_f32_f16_e32 v96, v97
	v_cvt_f32_f16_sdwa v97, v97 dst_sel:DWORD dst_unused:UNUSED_PAD src0_sel:WORD_1
	v_cvt_f32_f16_e32 v122, v98
	v_cvt_f32_f16_sdwa v123, v98 dst_sel:DWORD dst_unused:UNUSED_PAD src0_sel:WORD_1
	v_cvt_f32_f16_e32 v98, v99
	v_cvt_f32_f16_sdwa v99, v99 dst_sel:DWORD dst_unused:UNUSED_PAD src0_sel:WORD_1
	v_pk_fma_f32 v[6:7], v[100:101], v[108:109], v[6:7] op_sel_hi:[0,1,1]
	v_pk_fma_f32 v[8:9], v[100:101], v[84:85], v[8:9] op_sel_hi:[0,1,1]
	v_pk_fma_f32 v[2:3], v[100:101], v[110:111], v[2:3] op_sel_hi:[0,1,1]
	v_pk_fma_f32 v[4:5], v[100:101], v[86:87], v[4:5] op_sel_hi:[0,1,1]
	v_pk_fma_f32 v[6:7], v[102:103], v[112:113], v[6:7] op_sel_hi:[0,1,1]
	v_pk_fma_f32 v[8:9], v[102:103], v[88:89], v[8:9] op_sel_hi:[0,1,1]
	v_pk_fma_f32 v[2:3], v[102:103], v[114:115], v[2:3] op_sel_hi:[0,1,1]
	v_pk_fma_f32 v[4:5], v[102:103], v[90:91], v[4:5] op_sel_hi:[0,1,1]
	s_add_i32 s7, s7, 16
	v_pk_fma_f32 v[6:7], v[104:105], v[116:117], v[6:7] op_sel_hi:[0,1,1]
	v_pk_fma_f32 v[8:9], v[104:105], v[92:93], v[8:9] op_sel_hi:[0,1,1]
	v_pk_fma_f32 v[2:3], v[104:105], v[118:119], v[2:3] op_sel_hi:[0,1,1]
	v_pk_fma_f32 v[4:5], v[104:105], v[94:95], v[4:5] op_sel_hi:[0,1,1]
	v_add_u32_e32 v12, 4, v12
	s_cmp_eq_u32 s7, 64
	s_waitcnt lgkmcnt(0)
	v_pk_fma_f32 v[6:7], v[106:107], v[120:121], v[6:7] op_sel_hi:[0,1,1]
	v_pk_fma_f32 v[8:9], v[106:107], v[96:97], v[8:9] op_sel_hi:[0,1,1]
	v_pk_fma_f32 v[2:3], v[106:107], v[122:123], v[2:3] op_sel_hi:[0,1,1]
	v_pk_fma_f32 v[4:5], v[106:107], v[98:99], v[4:5] op_sel_hi:[0,1,1]
	s_cbranch_scc0 .LBB5_167
	v_lshlrev_b32_e32 v80, 11, v187
	s_add_i32 s2, 0, 0x22240
	v_lshlrev_b32_e32 v12, 5, v189
	v_add3_u32 v80, s2, v80, v12
	ds_write_b128 v80, v[6:9]
	ds_write_b128 v80, v[2:5] offset:16
	v_add_u32_e32 v8, s2, v185
	s_waitcnt lgkmcnt(0)
	s_barrier
	ds_read2st64_b32 v[2:3], v8 offset1:8
	ds_read2st64_b32 v[4:5], v8 offset0:16 offset1:24
	ds_read2st64_b32 v[6:7], v8 offset0:32 offset1:40
	s_add_i32 s2, 0, 0x21200
	v_lshl_add_u32 v70, v70, 2, s2
	s_waitcnt lgkmcnt(2)
	v_add_f32_e32 v2, 0, v2
	v_add_f32_e32 v9, v2, v3
	ds_read2st64_b32 v[2:3], v8 offset0:48 offset1:56
	s_waitcnt lgkmcnt(2)
	v_add_f32_e32 v4, v9, v4
	v_add_f32_e32 v4, v4, v5
	s_waitcnt lgkmcnt(1)
	v_add_f32_e32 v4, v4, v6
	v_add_f32_e32 v4, v4, v7
	s_waitcnt lgkmcnt(0)
	v_add_f32_e32 v2, v4, v2
	v_add_f32_e32 v2, v2, v3
	v_add_u32_e32 v3, s2, v185
	ds_write_b32 v3, v2
	s_waitcnt lgkmcnt(0)
	s_barrier
	ds_read_b128 v[2:5], v70
	ds_read_b128 v[6:9], v70 offset:16
	ds_read_b128 v[80:83], v70 offset:32
	ds_read_b128 v[84:87], v70 offset:48
	s_waitcnt lgkmcnt(3)
	v_fma_f32 v78, v78, v2, 0
	s_waitcnt vmcnt(62)
	v_fmac_f32_e32 v78, v77, v3
	s_waitcnt vmcnt(61)
	v_fmac_f32_e32 v78, v76, v4
	s_waitcnt vmcnt(60)
	v_fmac_f32_e32 v78, v75, v5
	s_waitcnt vmcnt(59) lgkmcnt(2)
	v_fmac_f32_e32 v78, v74, v6
	s_waitcnt vmcnt(58)
	v_fmac_f32_e32 v78, v73, v7
	s_waitcnt vmcnt(57)
	v_fmac_f32_e32 v78, v72, v8
	s_waitcnt vmcnt(56)
	v_fmac_f32_e32 v78, v71, v9
	s_waitcnt vmcnt(55) lgkmcnt(1)
	v_fmac_f32_e32 v78, v69, v80
	s_waitcnt vmcnt(54)
	v_fmac_f32_e32 v78, v65, v81
	s_waitcnt vmcnt(53)
	v_fmac_f32_e32 v78, v63, v82
	s_waitcnt vmcnt(52)
	v_fmac_f32_e32 v78, v62, v83
	ds_read_b128 v[2:5], v70 offset:64
	ds_read_b128 v[6:9], v70 offset:80
	s_waitcnt vmcnt(51) lgkmcnt(2)
	v_fmac_f32_e32 v78, v61, v84
	s_waitcnt vmcnt(50)
	v_fmac_f32_e32 v78, v51, v85
	s_waitcnt vmcnt(49)
	v_fmac_f32_e32 v78, v52, v86
	s_waitcnt vmcnt(48)
	v_fmac_f32_e32 v78, v53, v87
	s_waitcnt vmcnt(7) lgkmcnt(1)
	v_fmac_f32_e32 v78, v79, v2
	v_fmac_f32_e32 v78, v55, v3
	v_fmac_f32_e32 v78, v56, v4
	v_fmac_f32_e32 v78, v57, v5
	ds_read_b128 v[2:5], v70 offset:96
	s_waitcnt lgkmcnt(1)
	v_fmac_f32_e32 v78, v54, v6
	v_fmac_f32_e32 v78, v48, v7
	v_fmac_f32_e32 v78, v49, v8
	v_fmac_f32_e32 v78, v50, v9
	ds_read_b128 v[6:9], v70 offset:112
	s_waitcnt lgkmcnt(1)
	v_fmac_f32_e32 v78, v47, v2
	v_fmac_f32_e32 v78, v66, v3
	v_fmac_f32_e32 v78, v67, v4
	v_fmac_f32_e32 v78, v68, v5
	ds_read_b128 v[2:5], v70 offset:128
	s_waitcnt lgkmcnt(1)
	v_fmac_f32_e32 v78, v64, v6
	v_fmac_f32_e32 v78, v58, v7
	v_fmac_f32_e32 v78, v59, v8
	v_fmac_f32_e32 v78, v60, v9
	ds_read_b128 v[6:9], v70 offset:144
	s_waitcnt lgkmcnt(1)
	v_fmac_f32_e32 v78, v43, v2
	v_fmac_f32_e32 v78, v44, v3
	v_fmac_f32_e32 v78, v45, v4
	v_fmac_f32_e32 v78, v46, v5
	ds_read_b128 v[2:5], v70 offset:160
	s_waitcnt lgkmcnt(1)
	v_fmac_f32_e32 v78, v42, v6
	v_fmac_f32_e32 v78, v39, v7
	v_fmac_f32_e32 v78, v40, v8
	v_fmac_f32_e32 v78, v41, v9
	ds_read_b128 v[6:9], v70 offset:176
	s_waitcnt lgkmcnt(1)
	v_fmac_f32_e32 v78, v33, v2
	v_fmac_f32_e32 v78, v34, v3
	v_fmac_f32_e32 v78, v35, v4
	v_fmac_f32_e32 v78, v36, v5
	ds_read_b128 v[2:5], v70 offset:192
	s_waitcnt lgkmcnt(1)
	v_fmac_f32_e32 v78, v32, v6
	v_fmac_f32_e32 v78, v24, v7
	v_fmac_f32_e32 v78, v25, v8
	v_fmac_f32_e32 v78, v26, v9
	ds_read_b128 v[6:9], v70 offset:208
	s_waitcnt lgkmcnt(1)
	v_fmac_f32_e32 v78, v28, v2
	v_fmac_f32_e32 v78, v29, v3
	v_fmac_f32_e32 v78, v30, v4
	v_fmac_f32_e32 v78, v31, v5
	ds_read_b128 v[2:5], v70 offset:224
	s_waitcnt lgkmcnt(1)
	v_fmac_f32_e32 v78, v27, v6
	v_fmac_f32_e32 v78, v21, v7
	v_fmac_f32_e32 v78, v22, v8
	v_fmac_f32_e32 v78, v23, v9
	ds_read_b128 v[6:9], v70 offset:240
	s_waitcnt lgkmcnt(1)
	v_fmac_f32_e32 v78, v16, v2
	s_waitcnt vmcnt(6)
	v_fmac_f32_e32 v78, v18, v3
	s_waitcnt vmcnt(5)
	v_fmac_f32_e32 v78, v19, v4
	s_waitcnt vmcnt(4)
	v_fmac_f32_e32 v78, v20, v5
	s_waitcnt vmcnt(3) lgkmcnt(0)
	v_fmac_f32_e32 v78, v17, v6
	s_waitcnt vmcnt(2)
	v_fmac_f32_e32 v78, v15, v7
	s_waitcnt vmcnt(1)
	v_fmac_f32_e32 v78, v13, v8
	v_add_u32_e32 v2, 0, v185
	s_waitcnt vmcnt(0)
	v_fmac_f32_e32 v78, v11, v9
	v_add_u32_e32 v2, 0x20000, v2
	ds_write_b32 v2, v78
	s_waitcnt lgkmcnt(0)
	s_barrier
	s_and_saveexec_b64 s[2:3], s[0:1]
	s_cbranch_execz .LBB5_170
	ds_read2st64_b32 v[4:5], v2 offset1:1
	ds_read2st64_b32 v[6:7], v2 offset0:2 offset1:3
	ds_read2st64_b32 v[8:9], v2 offset0:4 offset1:5
	ds_read2st64_b32 v[2:3], v2 offset0:6 offset1:7
	s_lshl_b64 s[12:13], s[34:35], 11
	s_waitcnt lgkmcnt(3)
	v_add_f32_e32 v4, 0, v4
	v_add_f32_e32 v4, v4, v5
	s_waitcnt lgkmcnt(2)
	v_add_f32_e32 v4, v4, v6
	v_add_f32_e32 v4, v4, v7
	s_waitcnt lgkmcnt(1)
	v_add_f32_e32 v4, v4, v8
	s_add_u32 s7, s20, s12
	v_add_f32_e32 v4, v4, v9
	s_addc_u32 s13, s21, s13
	s_lshl_b32 s12, s33, 8
	s_waitcnt lgkmcnt(0)
	v_add_f32_e32 v2, v4, v2
	s_add_u32 s12, s7, s12
	v_add_f32_e32 v2, v2, v3
	s_addc_u32 s13, s13, 0
	s_nop 1
	v_mov_b32_dpp v4, v2 quad_perm:[0,0,0,0] row_mask:0xf bank_mask:0xf
	v_mov_b32_dpp v5, v2 quad_perm:[1,1,1,1] row_mask:0xf bank_mask:0xf
	v_mov_b32_dpp v6, v2 quad_perm:[2,2,2,2] row_mask:0xf bank_mask:0xf
	v_mov_b32_dpp v7, v2 quad_perm:[3,3,3,3] row_mask:0xf bank_mask:0xf
	v_and_b32_e32 v8, 3, v189
	v_cmp_eq_u32_e32 vcc, 0, v8
	s_and_b64 exec, exec, vcc
	global_store_dwordx4 v185, v[4:7], s[12:13] sc1
.LBB5_170:
	s_or_b64 exec, exec, s[2:3]
	s_and_saveexec_b64 s[2:3], s[4:5]
	s_cbranch_execz .LBB5_172
	s_lshl_b32 s7, s33, 1
	s_lshl_b32 s12, s34, 4
	s_or_b32 s12, s12, s7
	s_ashr_i32 s13, s12, 31
	s_lshl_b64 s[12:13], s[12:13], 2
	s_add_u32 s12, s22, s12
	s_addc_u32 s13, s23, s13
	v_mov_b32_e32 v3, 0
	v_add_f32_e32 v2, v37, v38
	v_mov_b32_e32 v4, v14
	v_mov_b32_e32 v5, v2
	global_store_dwordx2 v3, v[4:5], s[12:13] sc1
